# P2 fp8 GEMM: next tile's late A piece LDS-DMA issued before the epilogue stores; first K-iteration's counted wait allows the 16 stores outstanding
# speedup vs baseline: 1.0061x; 1.0003x over previous
.LBB0_198:
	s_lshl_b32 s6, s6, 5
	s_and_b32 s20, s6, 0x60
	s_mov_b64 s[6:7], 0x80
	s_add_i32 m0, s29, 0x18000
	v_lshl_add_u64 v[8:9], v[8:9], 0, s[6:7]
	s_lshl_b32 s8, s1, 13
	s_lshl_b32 s21, s20, 7
	s_waitcnt vmcnt(4)
	s_barrier
	global_load_lds_dwordx4 v[8:9], off
	v_lshl_add_u64 v[6:7], v[6:7], 0, s[6:7]
	s_add_i32 m0, s29, 0x1a000
	s_add_i32 s45, s29, 0x8000
	s_add_i32 s46, s29, 0xa000
	global_load_lds_dwordx4 v[6:7], off
	v_lshl_add_u64 v[4:5], v[4:5], 0, s[6:7]
	s_mov_b32 m0, s45
	s_add_u32 s10, s34, 0x40080
	global_load_lds_dwordx4 v[4:5], off
	v_lshl_add_u64 v[2:3], v[2:3], 0, s[6:7]
	s_mov_b32 m0, s46
	s_addc_u32 s11, s35, 0
	global_load_lds_dwordx4 v[2:3], off
	s_add_i32 m0, s29, 0x1c000
	v_lshl_add_u64 v[2:3], s[10:11], 0, v[150:151]
	global_load_lds_dwordx4 v[2:3], off
	v_lshl_add_u64 v[2:3], s[10:11], 0, v[146:147]
	s_add_i32 m0, s29, 0x1e000
	s_sext_i32_i16 s51, s0
	global_load_lds_dwordx4 v[2:3], off
	s_add_u32 s60, s30, 0x40080
	s_addc_u32 s61, s31, 0
	v_lshl_add_u64 v[2:3], s[60:61], 0, v[152:153]
	s_add_i32 m0, s29, 0xc000
	s_nop 0
	global_load_lds_dwordx4 v[2:3], off
	v_lshl_add_u64 v[2:3], s[60:61], 0, v[148:149]
	s_add_i32 m0, s29, 0xe000
	s_nop 0
	global_load_lds_dwordx4 v[2:3], off
	v_and_b32_e32 v2, 15, v0
	v_lshlrev_b32_e32 v3, 1, v13
	v_lshlrev_b32_e32 v4, 2, v0
	v_lshlrev_b32_e32 v5, 6, v0
	s_movk_i32 s0, 0x3c0
	v_lshl_or_b32 v1, s1, 6, v2
	v_lshl_or_b32 v2, v2, 6, v3
	v_and_b32_e32 v4, 32, v4
	v_and_or_b32 v3, v5, s0, v3
	v_bitop3_b32 v170, s21, v3, v4 bitop3:0xf6
	v_lshlrev_b32_e32 v3, 8, v0
	v_bitop3_b32 v2, v2, s8, v4 bitop3:0xde
	v_and_b32_e32 v3, 0x18000, v3
	v_lshlrev_b32_e32 v4, 11, v14
	v_or3_b32 v3, v11, v3, v4
	v_add_u32_e32 v154, v3, v12
	v_lshlrev_b32_e32 v3, 4, v10
	s_waitcnt vmcnt(6)
	v_and_b32_e32 v3, 0x38000, v3
	v_or3_b32 v3, v11, v3, v4
	s_add_i32 s48, 0, 0x10000
	s_add_i32 s49, 0, 0x14000
	s_ashr_i32 s47, s92, 31
	v_or_b32_e32 v171, s20, v13
	v_mov_b32_e32 v155, v151
	v_add_u32_e32 v156, v3, v12
	v_mov_b32_e32 v157, v151
	v_mov_b64_e32 v[158:159], 0xea0
	v_mov_b64_e32 v[160:161], 0xe9f
	v_add_u32_e32 v172, s48, v170
	v_add_u32_e32 v173, 0, v2
	v_mov_b32_e32 v174, 0x7f7f7f7f
	v_add_u32_e32 v175, s49, v170
	s_movk_i32 s50, 0x3400
	s_brev_b32 s8, 28
	s_barrier
	s_waitcnt vmcnt(0)

.LBB0_202:
	ds_read_b128 v[2:5], v172
	ds_read_b128 v[6:9], v172 offset:1024
	ds_read_b128 v[10:13], v172 offset:2048
	ds_read_b128 v[14:17], v172 offset:3072
	s_add_u32 s34, s30, 0xfffc0080
	s_addc_u32 s35, s31, -1
	s_cmp_eq_u32 s56, 12
	s_cselect_b32 s37, s21, s35
	s_cselect_b32 s36, s52, s34
	s_cselect_b32 s35, s11, s55
	s_cselect_b32 s34, s53, s54
	v_lshl_add_u64 v[162:163], s[30:31], 0, v[154:155]
	s_add_i32 m0, s29, 0xc000
	ds_read_b128 v[176:179], v173
	ds_read_b128 v[180:183], v173 offset:1024
	ds_read_b128 v[184:187], v173 offset:2048
	ds_read_b128 v[188:191], v173 offset:3072
	ds_read_b128 v[192:195], v173 offset:4096
	ds_read_b128 v[196:199], v173 offset:5120
	ds_read_b128 v[206:209], v173 offset:6144
	ds_read_b128 v[210:213], v173 offset:7168
	s_cmp_eq_u32 s56, -2
	s_cbranch_scc1 .Lp2h_a
	global_load_lds_dwordx4 v[162:163], off
.Lp2h_a:
	v_lshl_add_u64 v[162:163], s[30:31], 0, v[156:157]
	s_add_i32 m0, s29, 0xe000
	s_nop 0
	s_cmp_eq_u32 s56, -2
	s_cbranch_scc1 .Lp2h_b
	global_load_lds_dwordx4 v[162:163], off
.Lp2h_b:
	s_waitcnt lgkmcnt(8)
	s_barrier
	s_waitcnt lgkmcnt(0)
	s_setprio 1
	s_waitcnt lgkmcnt(0)
	v_mfma_scale_f32_16x16x128_f8f6f4 v[142:145], v[2:9], v[176:183], v[142:145], v174, v174 op_sel_hi:[0,0,0]
	v_mfma_scale_f32_16x16x128_f8f6f4 v[138:141], v[10:17], v[176:183], v[138:141], v174, v174 op_sel_hi:[0,0,0]
	v_mfma_scale_f32_16x16x128_f8f6f4 v[134:137], v[2:9], v[184:191], v[134:137], v174, v174 op_sel_hi:[0,0,0]
	v_mfma_scale_f32_16x16x128_f8f6f4 v[126:129], v[10:17], v[184:191], v[126:129], v174, v174 op_sel_hi:[0,0,0]
	v_mfma_scale_f32_16x16x128_f8f6f4 v[118:121], v[2:9], v[192:199], v[118:121], v174, v174 op_sel_hi:[0,0,0]
	v_mfma_scale_f32_16x16x128_f8f6f4 v[110:113], v[10:17], v[192:199], v[110:113], v174, v174 op_sel_hi:[0,0,0]
	v_mfma_scale_f32_16x16x128_f8f6f4 v[102:105], v[2:9], v[206:213], v[102:105], v174, v174 op_sel_hi:[0,0,0]
	v_mfma_scale_f32_16x16x128_f8f6f4 v[94:97], v[10:17], v[206:213], v[94:97], v174, v174 op_sel_hi:[0,0,0]
	s_setprio 0
	s_barrier
	s_add_i32 s57, s48, s38
	v_lshl_add_u64 v[162:163], s[34:35], 0, v[150:151]
	s_mov_b32 m0, s57
	ds_read_b128 v[214:217], v175
	ds_read_b128 v[218:221], v175 offset:1024
	ds_read_b128 v[222:225], v175 offset:2048
	ds_read_b128 v[226:229], v175 offset:3072
	global_load_lds_dwordx4 v[162:163], off
	v_lshl_add_u64 v[164:165], s[34:35], 0, v[146:147]
	s_add_i32 m0, s57, 0x2000
	s_nop 0
	global_load_lds_dwordx4 v[164:165], off
	s_barrier
	s_waitcnt lgkmcnt(0)
	s_setprio 1
	s_waitcnt lgkmcnt(0)
	v_mfma_scale_f32_16x16x128_f8f6f4 v[130:133], v[214:221], v[176:183], v[130:133], v174, v174 op_sel_hi:[0,0,0]
	v_mfma_scale_f32_16x16x128_f8f6f4 v[122:125], v[222:229], v[176:183], v[122:125], v174, v174 op_sel_hi:[0,0,0]
	v_mfma_scale_f32_16x16x128_f8f6f4 v[114:117], v[214:221], v[184:191], v[114:117], v174, v174 op_sel_hi:[0,0,0]
	v_mfma_scale_f32_16x16x128_f8f6f4 v[106:109], v[222:229], v[184:191], v[106:109], v174, v174 op_sel_hi:[0,0,0]
	v_mfma_scale_f32_16x16x128_f8f6f4 v[98:101], v[214:221], v[192:199], v[98:101], v174, v174 op_sel_hi:[0,0,0]
	v_mfma_scale_f32_16x16x128_f8f6f4 v[90:93], v[222:229], v[192:199], v[90:93], v174, v174 op_sel_hi:[0,0,0]
	v_mfma_scale_f32_16x16x128_f8f6f4 v[86:89], v[214:221], v[206:213], v[86:89], v174, v174 op_sel_hi:[0,0,0]
	v_mfma_scale_f32_16x16x128_f8f6f4 v[82:85], v[222:229], v[206:213], v[82:85], v174, v174 op_sel_hi:[0,0,0]
	s_setprio 0
	s_mov_b32 m0, s29
	v_lshl_add_u64 v[166:167], s[36:37], 0, v[152:153]
	s_barrier
	ds_read_b128 v[176:179], v173 offset:16384
	ds_read_b128 v[180:183], v173 offset:17408
	ds_read_b128 v[184:187], v173 offset:18432
	ds_read_b128 v[188:191], v173 offset:19456
	ds_read_b128 v[192:195], v173 offset:20480
	ds_read_b128 v[196:199], v173 offset:21504
	ds_read_b128 v[206:209], v173 offset:22528
	ds_read_b128 v[210:213], v173 offset:23552
	global_load_lds_dwordx4 v[166:167], off
	v_lshl_add_u64 v[168:169], s[36:37], 0, v[148:149]
	s_mov_b32 m0, s41
	s_nop 0
	global_load_lds_dwordx4 v[168:169], off
	s_barrier
	s_waitcnt lgkmcnt(0)
	s_setprio 1
	s_waitcnt lgkmcnt(0)
	v_mfma_scale_f32_16x16x128_f8f6f4 v[78:81], v[2:9], v[176:183], v[78:81], v174, v174 op_sel_hi:[0,0,0]
	v_mfma_scale_f32_16x16x128_f8f6f4 v[74:77], v[10:17], v[176:183], v[74:77], v174, v174 op_sel_hi:[0,0,0]
	v_mfma_scale_f32_16x16x128_f8f6f4 v[70:73], v[2:9], v[184:191], v[70:73], v174, v174 op_sel_hi:[0,0,0]
	v_mfma_scale_f32_16x16x128_f8f6f4 v[62:65], v[10:17], v[184:191], v[62:65], v174, v174 op_sel_hi:[0,0,0]
	v_mfma_scale_f32_16x16x128_f8f6f4 v[54:57], v[2:9], v[192:199], v[54:57], v174, v174 op_sel_hi:[0,0,0]
	v_mfma_scale_f32_16x16x128_f8f6f4 v[46:49], v[10:17], v[192:199], v[46:49], v174, v174 op_sel_hi:[0,0,0]
	v_mfma_scale_f32_16x16x128_f8f6f4 v[38:41], v[2:9], v[206:213], v[38:41], v174, v174 op_sel_hi:[0,0,0]
	v_mfma_scale_f32_16x16x128_f8f6f4 v[30:33], v[10:17], v[206:213], v[30:33], v174, v174 op_sel_hi:[0,0,0]
	s_setprio 0
	s_barrier
	s_add_u32 s60, s34, 0x40000
	s_addc_u32 s61, s35, 0
	s_add_i32 s57, s49, s38
	v_lshl_add_u64 v[2:3], s[60:61], 0, v[150:151]
	s_mov_b32 m0, s57
	s_nop 0
	global_load_lds_dwordx4 v[2:3], off
	v_lshl_add_u64 v[2:3], s[60:61], 0, v[146:147]
	s_add_i32 m0, s57, 0x2000
	s_nop 0
	global_load_lds_dwordx4 v[2:3], off
	s_cmp_eq_u32 s56, -2
	s_cbranch_scc1 .Lp2h_c
	s_waitcnt vmcnt(6)
	s_branch .Lp2h_d
.Lp2h_c:
	s_waitcnt vmcnt(22)
.Lp2h_d:
	s_barrier
	s_setprio 1
	v_mfma_scale_f32_16x16x128_f8f6f4 v[66:69], v[214:221], v[176:183], v[66:69], v174, v174 op_sel_hi:[0,0,0]
	v_mfma_scale_f32_16x16x128_f8f6f4 v[58:61], v[222:229], v[176:183], v[58:61], v174, v174 op_sel_hi:[0,0,0]
	v_mfma_scale_f32_16x16x128_f8f6f4 v[50:53], v[214:221], v[184:191], v[50:53], v174, v174 op_sel_hi:[0,0,0]
	v_mfma_scale_f32_16x16x128_f8f6f4 v[42:45], v[222:229], v[184:191], v[42:45], v174, v174 op_sel_hi:[0,0,0]
	v_mfma_scale_f32_16x16x128_f8f6f4 v[34:37], v[214:221], v[192:199], v[34:37], v174, v174 op_sel_hi:[0,0,0]
	v_mfma_scale_f32_16x16x128_f8f6f4 v[26:29], v[222:229], v[192:199], v[26:29], v174, v174 op_sel_hi:[0,0,0]
	v_mfma_scale_f32_16x16x128_f8f6f4 v[22:25], v[214:221], v[206:213], v[22:25], v174, v174 op_sel_hi:[0,0,0]
	v_mfma_scale_f32_16x16x128_f8f6f4 v[18:21], v[222:229], v[206:213], v[18:21], v174, v174 op_sel_hi:[0,0,0]
	s_setprio 0
	s_add_i32 s57, 0, 0x18000
	v_add_u32_e32 v14, s57, v170
	s_barrier
	ds_read_b128 v[2:5], v14
	ds_read_b128 v[6:9], v14 offset:1024
	ds_read_b128 v[10:13], v14 offset:2048
	ds_read_b128 v[14:17], v14 offset:3072
	s_add_u32 s36, s36, 0x40000
	s_addc_u32 s37, s37, 0
	s_mov_b32 m0, s42
	v_lshl_add_u64 v[200:201], s[36:37], 0, v[152:153]
	ds_read_b128 v[176:179], v173 offset:32768
	ds_read_b128 v[180:183], v173 offset:33792
	ds_read_b128 v[184:187], v173 offset:34816
	ds_read_b128 v[188:191], v173 offset:35840
	ds_read_b128 v[192:195], v173 offset:36864
	ds_read_b128 v[196:199], v173 offset:37888
	ds_read_b128 v[206:209], v173 offset:38912
	ds_read_b128 v[210:213], v173 offset:39936
	global_load_lds_dwordx4 v[200:201], off
	v_lshl_add_u64 v[200:201], s[36:37], 0, v[148:149]
	s_mov_b32 m0, s43
	s_nop 0
	global_load_lds_dwordx4 v[200:201], off
	s_waitcnt lgkmcnt(8)
	s_barrier
	s_waitcnt lgkmcnt(0)
	s_setprio 1
	s_waitcnt lgkmcnt(0)
	v_mfma_scale_f32_16x16x128_f8f6f4 v[142:145], v[2:9], v[176:183], v[142:145], v174, v174 op_sel_hi:[0,0,0]
	v_mfma_scale_f32_16x16x128_f8f6f4 v[138:141], v[10:17], v[176:183], v[138:141], v174, v174 op_sel_hi:[0,0,0]
	v_mfma_scale_f32_16x16x128_f8f6f4 v[134:137], v[2:9], v[184:191], v[134:137], v174, v174 op_sel_hi:[0,0,0]
	v_mfma_scale_f32_16x16x128_f8f6f4 v[126:129], v[10:17], v[184:191], v[126:129], v174, v174 op_sel_hi:[0,0,0]
	v_mfma_scale_f32_16x16x128_f8f6f4 v[118:121], v[2:9], v[192:199], v[118:121], v174, v174 op_sel_hi:[0,0,0]
	v_mfma_scale_f32_16x16x128_f8f6f4 v[110:113], v[10:17], v[192:199], v[110:113], v174, v174 op_sel_hi:[0,0,0]
	v_mfma_scale_f32_16x16x128_f8f6f4 v[102:105], v[2:9], v[206:213], v[102:105], v174, v174 op_sel_hi:[0,0,0]
	v_mfma_scale_f32_16x16x128_f8f6f4 v[94:97], v[10:17], v[206:213], v[94:97], v174, v174 op_sel_hi:[0,0,0]
	s_setprio 0
	s_barrier
	s_add_i32 s36, 0, 0x1c000
	s_add_i32 s37, s57, s38
	v_add_u32_e32 v200, s36, v170
	v_lshl_add_u64 v[162:163], v[162:163], 0, s[6:7]
	s_mov_b32 m0, s37
	ds_read_b128 v[214:217], v200
	ds_read_b128 v[218:221], v200 offset:1024
	ds_read_b128 v[222:225], v200 offset:2048
	ds_read_b128 v[226:229], v200 offset:3072
	global_load_lds_dwordx4 v[162:163], off
	v_lshl_add_u64 v[162:163], v[164:165], 0, s[6:7]
	s_add_i32 m0, s37, 0x2000
	s_nop 0
	global_load_lds_dwordx4 v[162:163], off
	s_barrier
	s_waitcnt lgkmcnt(0)
	s_setprio 1
	s_waitcnt lgkmcnt(0)
	v_mfma_scale_f32_16x16x128_f8f6f4 v[130:133], v[214:221], v[176:183], v[130:133], v174, v174 op_sel_hi:[0,0,0]
	v_mfma_scale_f32_16x16x128_f8f6f4 v[122:125], v[222:229], v[176:183], v[122:125], v174, v174 op_sel_hi:[0,0,0]
	v_mfma_scale_f32_16x16x128_f8f6f4 v[114:117], v[214:221], v[184:191], v[114:117], v174, v174 op_sel_hi:[0,0,0]
	v_mfma_scale_f32_16x16x128_f8f6f4 v[106:109], v[222:229], v[184:191], v[106:109], v174, v174 op_sel_hi:[0,0,0]
	v_mfma_scale_f32_16x16x128_f8f6f4 v[98:101], v[214:221], v[192:199], v[98:101], v174, v174 op_sel_hi:[0,0,0]
	v_mfma_scale_f32_16x16x128_f8f6f4 v[90:93], v[222:229], v[192:199], v[90:93], v174, v174 op_sel_hi:[0,0,0]
	v_mfma_scale_f32_16x16x128_f8f6f4 v[86:89], v[214:221], v[206:213], v[86:89], v174, v174 op_sel_hi:[0,0,0]
	v_mfma_scale_f32_16x16x128_f8f6f4 v[82:85], v[222:229], v[206:213], v[82:85], v174, v174 op_sel_hi:[0,0,0]
	s_setprio 0
	s_mov_b32 m0, s45
	v_lshl_add_u64 v[162:163], v[166:167], 0, s[6:7]
	s_barrier
	ds_read_b128 v[176:179], v173 offset:49152
	ds_read_b128 v[180:183], v173 offset:50176
	ds_read_b128 v[184:187], v173 offset:51200
	ds_read_b128 v[188:191], v173 offset:52224
	ds_read_b128 v[192:195], v173 offset:53248
	ds_read_b128 v[196:199], v173 offset:54272
	ds_read_b128 v[206:209], v173 offset:55296
	ds_read_b128 v[210:213], v173 offset:56320
	global_load_lds_dwordx4 v[162:163], off
	v_lshl_add_u64 v[162:163], v[168:169], 0, s[6:7]
	s_mov_b32 m0, s46
	s_nop 0
	global_load_lds_dwordx4 v[162:163], off
	s_barrier
	s_waitcnt lgkmcnt(0)
	s_setprio 1
	s_waitcnt lgkmcnt(0)
	v_mfma_scale_f32_16x16x128_f8f6f4 v[78:81], v[2:9], v[176:183], v[78:81], v174, v174 op_sel_hi:[0,0,0]
	v_mfma_scale_f32_16x16x128_f8f6f4 v[74:77], v[10:17], v[176:183], v[74:77], v174, v174 op_sel_hi:[0,0,0]
	v_mfma_scale_f32_16x16x128_f8f6f4 v[70:73], v[2:9], v[184:191], v[70:73], v174, v174 op_sel_hi:[0,0,0]
	v_mfma_scale_f32_16x16x128_f8f6f4 v[62:65], v[10:17], v[184:191], v[62:65], v174, v174 op_sel_hi:[0,0,0]
	v_mfma_scale_f32_16x16x128_f8f6f4 v[54:57], v[2:9], v[192:199], v[54:57], v174, v174 op_sel_hi:[0,0,0]
	v_mfma_scale_f32_16x16x128_f8f6f4 v[46:49], v[10:17], v[192:199], v[46:49], v174, v174 op_sel_hi:[0,0,0]
	v_mfma_scale_f32_16x16x128_f8f6f4 v[38:41], v[2:9], v[206:213], v[38:41], v174, v174 op_sel_hi:[0,0,0]
	v_mfma_scale_f32_16x16x128_f8f6f4 v[30:33], v[10:17], v[206:213], v[30:33], v174, v174 op_sel_hi:[0,0,0]
	s_setprio 0
	s_barrier
	s_add_u32 s34, s34, 0x40080
	s_addc_u32 s35, s35, 0
	s_add_i32 s36, s36, s38
	v_lshl_add_u64 v[2:3], s[34:35], 0, v[150:151]
	s_mov_b32 m0, s36
	s_nop 0
	global_load_lds_dwordx4 v[2:3], off
	v_lshl_add_u64 v[2:3], s[34:35], 0, v[146:147]
	s_add_i32 m0, s36, 0x2000
	s_nop 0
	global_load_lds_dwordx4 v[2:3], off
	s_waitcnt vmcnt(6)
	s_barrier
	s_setprio 1
	v_mfma_scale_f32_16x16x128_f8f6f4 v[66:69], v[214:221], v[176:183], v[66:69], v174, v174 op_sel_hi:[0,0,0]
	v_mfma_scale_f32_16x16x128_f8f6f4 v[58:61], v[222:229], v[176:183], v[58:61], v174, v174 op_sel_hi:[0,0,0]
	v_mfma_scale_f32_16x16x128_f8f6f4 v[50:53], v[214:221], v[184:191], v[50:53], v174, v174 op_sel_hi:[0,0,0]
	v_mfma_scale_f32_16x16x128_f8f6f4 v[42:45], v[222:229], v[184:191], v[42:45], v174, v174 op_sel_hi:[0,0,0]
	v_mfma_scale_f32_16x16x128_f8f6f4 v[34:37], v[214:221], v[192:199], v[34:37], v174, v174 op_sel_hi:[0,0,0]
	v_mfma_scale_f32_16x16x128_f8f6f4 v[26:29], v[222:229], v[192:199], v[26:29], v174, v174 op_sel_hi:[0,0,0]
	v_mfma_scale_f32_16x16x128_f8f6f4 v[22:25], v[214:221], v[206:213], v[22:25], v174, v174 op_sel_hi:[0,0,0]
	v_mfma_scale_f32_16x16x128_f8f6f4 v[18:21], v[222:229], v[206:213], v[18:21], v174, v174 op_sel_hi:[0,0,0]
	s_setprio 0
	s_add_i32 s56, s56, 2
	s_add_u32 s30, s30, 0x100
	s_addc_u32 s31, s31, 0
	s_add_u32 s54, s54, 0x100
	s_addc_u32 s55, s55, 0
	s_cmp_gt_u32 s56, 13
	s_barrier
	s_cbranch_scc0 .LBB0_202
	s_mov_b64 s[60:61], 0x40080
	v_lshl_add_u64 v[162:163], v[166:167], 0, s[60:61]
	s_add_i32 m0, s29, 0xc000
	s_nop 0
	global_load_lds_dwordx4 v[162:163], off
	v_lshl_add_u64 v[162:163], v[168:169], 0, s[60:61]
	s_add_i32 m0, s29, 0xe000
	s_nop 0
	global_load_lds_dwordx4 v[162:163], off
	v_lshl_or_b32 v4, s51, 8, v171
	v_lshl_add_u32 v16, s28, 8, v1
	v_ashrrev_i32_e32 v5, 31, v4
	v_mov_b64_e32 v[2:3], s[96:97]
	v_mad_i64_i32 v[6:7], s[30:31], v16, s50, v[2:3]
	v_lshlrev_b64 v[4:5], 1, v[4:5]
	v_lshl_add_u64 v[10:11], v[6:7], 0, v[4:5]
	v_pk_mul_f32 v[8:9], v[144:145], s[8:9] op_sel_hi:[1,0]
	v_pk_mul_f32 v[6:7], v[142:143], s[8:9] op_sel_hi:[1,0]
	v_pk_mul_f32 v[12:13], v[140:141], s[8:9] op_sel_hi:[1,0]
	v_pk_mul_f32 v[14:15], v[138:139], s[8:9] op_sel_hi:[1,0]
	v_cvt_pk_bf16_f32 v6, v6, v7
	v_cvt_pk_bf16_f32 v7, v8, v9
	v_cvt_pk_bf16_f32 v8, v14, v15
	v_cvt_pk_bf16_f32 v9, v12, v13
	global_store_dwordx4 v[10:11], v[6:9], off
	v_pk_mul_f32 v[12:13], v[124:125], s[8:9] op_sel_hi:[1,0]
	v_pk_mul_f32 v[14:15], v[122:123], s[8:9] op_sel_hi:[1,0]
	v_pk_mul_f32 v[8:9], v[132:133], s[8:9] op_sel_hi:[1,0]
	v_pk_mul_f32 v[6:7], v[130:131], s[8:9] op_sel_hi:[1,0]
	s_and_b64 vcc, exec, s[0:1]
	v_cvt_pk_bf16_f32 v6, v6, v7
	v_cvt_pk_bf16_f32 v7, v8, v9
	v_cvt_pk_bf16_f32 v8, v14, v15
	v_cvt_pk_bf16_f32 v9, v12, v13
	global_store_dwordx4 v[10:11], v[6:9], off offset:256
	v_pk_mul_f32 v[12:13], v[128:129], s[8:9] op_sel_hi:[1,0]
	v_pk_mul_f32 v[14:15], v[126:127], s[8:9] op_sel_hi:[1,0]
	v_or_b32_e32 v6, 16, v16
	v_mad_i64_i32 v[6:7], s[30:31], v6, s50, v[2:3]
	v_lshl_add_u64 v[10:11], v[6:7], 0, v[4:5]
	v_pk_mul_f32 v[8:9], v[136:137], s[8:9] op_sel_hi:[1,0]
	v_pk_mul_f32 v[6:7], v[134:135], s[8:9] op_sel_hi:[1,0]
	s_mov_b32 s51, s10
	v_cvt_pk_bf16_f32 v6, v6, v7
	v_cvt_pk_bf16_f32 v7, v8, v9
	v_cvt_pk_bf16_f32 v8, v14, v15
	v_cvt_pk_bf16_f32 v9, v12, v13
	global_store_dwordx4 v[10:11], v[6:9], off
	v_pk_mul_f32 v[12:13], v[108:109], s[8:9] op_sel_hi:[1,0]
	v_pk_mul_f32 v[14:15], v[106:107], s[8:9] op_sel_hi:[1,0]
	v_pk_mul_f32 v[8:9], v[116:117], s[8:9] op_sel_hi:[1,0]
	v_pk_mul_f32 v[6:7], v[114:115], s[8:9] op_sel_hi:[1,0]
	s_mov_b32 s28, s20
	v_cvt_pk_bf16_f32 v6, v6, v7
	v_cvt_pk_bf16_f32 v7, v8, v9
	v_cvt_pk_bf16_f32 v8, v14, v15
	v_cvt_pk_bf16_f32 v9, v12, v13
	global_store_dwordx4 v[10:11], v[6:9], off offset:256
	v_pk_mul_f32 v[12:13], v[112:113], s[8:9] op_sel_hi:[1,0]
	v_pk_mul_f32 v[14:15], v[110:111], s[8:9] op_sel_hi:[1,0]
	v_or_b32_e32 v6, 32, v16
	v_mad_i64_i32 v[6:7], s[30:31], v6, s50, v[2:3]
	v_lshl_add_u64 v[10:11], v[6:7], 0, v[4:5]
	v_pk_mul_f32 v[8:9], v[120:121], s[8:9] op_sel_hi:[1,0]
	v_pk_mul_f32 v[6:7], v[118:119], s[8:9] op_sel_hi:[1,0]
	s_mov_b64 s[34:35], s[26:27]
	v_cvt_pk_bf16_f32 v6, v6, v7
	v_cvt_pk_bf16_f32 v7, v8, v9
	v_cvt_pk_bf16_f32 v8, v14, v15
	v_cvt_pk_bf16_f32 v9, v12, v13
	global_store_dwordx4 v[10:11], v[6:9], off
	v_pk_mul_f32 v[12:13], v[92:93], s[8:9] op_sel_hi:[1,0]
	v_pk_mul_f32 v[14:15], v[90:91], s[8:9] op_sel_hi:[1,0]
	v_pk_mul_f32 v[8:9], v[100:101], s[8:9] op_sel_hi:[1,0]
	v_pk_mul_f32 v[6:7], v[98:99], s[8:9] op_sel_hi:[1,0]
	s_nop 0
	v_cvt_pk_bf16_f32 v6, v6, v7
	v_cvt_pk_bf16_f32 v7, v8, v9
	v_cvt_pk_bf16_f32 v8, v14, v15
	v_cvt_pk_bf16_f32 v9, v12, v13
	global_store_dwordx4 v[10:11], v[6:9], off offset:256
	v_pk_mul_f32 v[12:13], v[96:97], s[8:9] op_sel_hi:[1,0]
	v_pk_mul_f32 v[14:15], v[94:95], s[8:9] op_sel_hi:[1,0]
	v_or_b32_e32 v6, 48, v16
	v_mad_i64_i32 v[6:7], s[30:31], v6, s50, v[2:3]
	v_lshl_add_u64 v[10:11], v[6:7], 0, v[4:5]
	v_pk_mul_f32 v[8:9], v[104:105], s[8:9] op_sel_hi:[1,0]
	v_pk_mul_f32 v[6:7], v[102:103], s[8:9] op_sel_hi:[1,0]
	s_nop 0
	v_cvt_pk_bf16_f32 v6, v6, v7
	v_cvt_pk_bf16_f32 v7, v8, v9
	v_cvt_pk_bf16_f32 v8, v14, v15
	v_cvt_pk_bf16_f32 v9, v12, v13
	global_store_dwordx4 v[10:11], v[6:9], off
	v_pk_mul_f32 v[12:13], v[84:85], s[8:9] op_sel_hi:[1,0]
	v_pk_mul_f32 v[14:15], v[82:83], s[8:9] op_sel_hi:[1,0]
	v_pk_mul_f32 v[8:9], v[88:89], s[8:9] op_sel_hi:[1,0]
	v_pk_mul_f32 v[6:7], v[86:87], s[8:9] op_sel_hi:[1,0]
	s_nop 0
	v_cvt_pk_bf16_f32 v6, v6, v7
	v_cvt_pk_bf16_f32 v7, v8, v9
	v_cvt_pk_bf16_f32 v8, v14, v15
	v_cvt_pk_bf16_f32 v9, v12, v13
	global_store_dwordx4 v[10:11], v[6:9], off offset:256
	v_pk_mul_f32 v[12:13], v[76:77], s[8:9] op_sel_hi:[1,0]
	v_pk_mul_f32 v[14:15], v[74:75], s[8:9] op_sel_hi:[1,0]
	v_add_u32_e32 v6, 0x80, v16
	v_mad_i64_i32 v[6:7], s[30:31], v6, s50, v[2:3]
	v_lshl_add_u64 v[10:11], v[6:7], 0, v[4:5]
	v_pk_mul_f32 v[8:9], v[80:81], s[8:9] op_sel_hi:[1,0]
	v_pk_mul_f32 v[6:7], v[78:79], s[8:9] op_sel_hi:[1,0]
	s_nop 0
	v_cvt_pk_bf16_f32 v6, v6, v7
	v_cvt_pk_bf16_f32 v7, v8, v9
	v_cvt_pk_bf16_f32 v8, v14, v15
	v_cvt_pk_bf16_f32 v9, v12, v13
	global_store_dwordx4 v[10:11], v[6:9], off
	v_pk_mul_f32 v[12:13], v[60:61], s[8:9] op_sel_hi:[1,0]
	v_pk_mul_f32 v[14:15], v[58:59], s[8:9] op_sel_hi:[1,0]
	v_pk_mul_f32 v[8:9], v[68:69], s[8:9] op_sel_hi:[1,0]
	v_pk_mul_f32 v[6:7], v[66:67], s[8:9] op_sel_hi:[1,0]
	s_nop 0
	v_cvt_pk_bf16_f32 v6, v6, v7
	v_cvt_pk_bf16_f32 v7, v8, v9
	v_cvt_pk_bf16_f32 v8, v14, v15
	v_cvt_pk_bf16_f32 v9, v12, v13
	global_store_dwordx4 v[10:11], v[6:9], off offset:256
	v_pk_mul_f32 v[12:13], v[64:65], s[8:9] op_sel_hi:[1,0]
	v_pk_mul_f32 v[14:15], v[62:63], s[8:9] op_sel_hi:[1,0]
	v_add_u32_e32 v6, 0x90, v16
	v_mad_i64_i32 v[6:7], s[30:31], v6, s50, v[2:3]
	v_lshl_add_u64 v[10:11], v[6:7], 0, v[4:5]
	v_pk_mul_f32 v[8:9], v[72:73], s[8:9] op_sel_hi:[1,0]
	v_pk_mul_f32 v[6:7], v[70:71], s[8:9] op_sel_hi:[1,0]
	s_nop 0
	v_cvt_pk_bf16_f32 v6, v6, v7
	v_cvt_pk_bf16_f32 v7, v8, v9
	v_cvt_pk_bf16_f32 v8, v14, v15
	v_cvt_pk_bf16_f32 v9, v12, v13
	global_store_dwordx4 v[10:11], v[6:9], off
	v_pk_mul_f32 v[12:13], v[44:45], s[8:9] op_sel_hi:[1,0]
	v_pk_mul_f32 v[14:15], v[42:43], s[8:9] op_sel_hi:[1,0]
	v_pk_mul_f32 v[8:9], v[52:53], s[8:9] op_sel_hi:[1,0]
	v_pk_mul_f32 v[6:7], v[50:51], s[8:9] op_sel_hi:[1,0]
	s_nop 0
	v_cvt_pk_bf16_f32 v6, v6, v7
	v_cvt_pk_bf16_f32 v7, v8, v9
	v_cvt_pk_bf16_f32 v8, v14, v15
	v_cvt_pk_bf16_f32 v9, v12, v13
	global_store_dwordx4 v[10:11], v[6:9], off offset:256
	v_pk_mul_f32 v[12:13], v[48:49], s[8:9] op_sel_hi:[1,0]
	v_pk_mul_f32 v[14:15], v[46:47], s[8:9] op_sel_hi:[1,0]
	v_add_u32_e32 v6, 0xa0, v16
	v_mad_i64_i32 v[6:7], s[30:31], v6, s50, v[2:3]
	v_lshl_add_u64 v[10:11], v[6:7], 0, v[4:5]
	v_pk_mul_f32 v[8:9], v[56:57], s[8:9] op_sel_hi:[1,0]
	v_pk_mul_f32 v[6:7], v[54:55], s[8:9] op_sel_hi:[1,0]
	s_nop 0
	v_cvt_pk_bf16_f32 v6, v6, v7
	v_cvt_pk_bf16_f32 v7, v8, v9
	v_cvt_pk_bf16_f32 v8, v14, v15
	v_cvt_pk_bf16_f32 v9, v12, v13
	global_store_dwordx4 v[10:11], v[6:9], off
	v_pk_mul_f32 v[12:13], v[28:29], s[8:9] op_sel_hi:[1,0]
	v_pk_mul_f32 v[14:15], v[26:27], s[8:9] op_sel_hi:[1,0]
	v_pk_mul_f32 v[8:9], v[36:37], s[8:9] op_sel_hi:[1,0]
	v_pk_mul_f32 v[6:7], v[34:35], s[8:9] op_sel_hi:[1,0]
	s_nop 0
	v_cvt_pk_bf16_f32 v6, v6, v7
	v_cvt_pk_bf16_f32 v7, v8, v9
	v_cvt_pk_bf16_f32 v8, v14, v15
	v_cvt_pk_bf16_f32 v9, v12, v13
	global_store_dwordx4 v[10:11], v[6:9], off offset:256
	v_pk_mul_f32 v[10:11], v[30:31], s[8:9] op_sel_hi:[1,0]
	s_nop 0
	v_add_u32_e32 v6, 0xb0, v16
	v_mad_i64_i32 v[2:3], s[30:31], v6, s50, v[2:3]
	v_lshl_add_u64 v[6:7], v[2:3], 0, v[4:5]
	v_pk_mul_f32 v[4:5], v[40:41], s[8:9] op_sel_hi:[1,0]
	v_pk_mul_f32 v[2:3], v[38:39], s[8:9] op_sel_hi:[1,0]
	v_pk_mul_f32 v[8:9], v[32:33], s[8:9] op_sel_hi:[1,0]
	v_cvt_pk_bf16_f32 v2, v2, v3
	v_cvt_pk_bf16_f32 v3, v4, v5
	v_cvt_pk_bf16_f32 v4, v10, v11
	v_cvt_pk_bf16_f32 v5, v8, v9
	global_store_dwordx4 v[6:7], v[2:5], off
	v_pk_mul_f32 v[8:9], v[20:21], s[8:9] op_sel_hi:[1,0]
	v_pk_mul_f32 v[10:11], v[18:19], s[8:9] op_sel_hi:[1,0]
	v_pk_mul_f32 v[4:5], v[24:25], s[8:9] op_sel_hi:[1,0]
	v_pk_mul_f32 v[2:3], v[22:23], s[8:9] op_sel_hi:[1,0]
	s_mov_b64 s[30:31], s[22:23]
	v_cvt_pk_bf16_f32 v2, v2, v3
	v_cvt_pk_bf16_f32 v3, v4, v5
	v_cvt_pk_bf16_f32 v4, v10, v11
	v_cvt_pk_bf16_f32 v5, v8, v9
	global_store_dwordx4 v[6:7], v[2:5], off offset:256
	s_cbranch_vccz .LBB0_199
	s_waitcnt vmcnt(0)
	s_cmpk_gt_u32 s2, 0xff
	s_cbranch_scc1 .LBB0_206
	s_barrier
